# non-temporal stores for the converted fp8 weight tiles (mLSTM slot, attention host, MoE-1 epilogue host), on top of the single uniform mLSTM slot
# speedup vs baseline: 1.0111x; 1.0081x over previous
.Latt_cv_wd:
	s_lshr_b32 s100, s53, 8
	s_lshl_b32 s100, s100, 4
	s_add_i32 s100, s100, 16
	s_cmp_lt_u32 s99, s100
	s_cbranch_scc0 .Latt_cv_skip
	v_mul_f32_e32 v232, 0x42000000, v232
	v_mul_f32_e32 v236, 0x42000000, v236
	v_mul_f32_e32 v240, 0x42000000, v240
	v_mul_f32_e32 v244, 0x42000000, v244
	v_mov_b32_e32 v248, 0
	v_cvt_pk_fp8_f32 v248, v232, v236
	v_cvt_pk_fp8_f32 v248, v240, v244 op_sel:[0,0,1]
	v_mul_f32_e32 v233, 0x42000000, v233
	v_mul_f32_e32 v237, 0x42000000, v237
	v_mul_f32_e32 v241, 0x42000000, v241
	v_mul_f32_e32 v245, 0x42000000, v245
	v_mov_b32_e32 v249, 0
	v_cvt_pk_fp8_f32 v249, v233, v237
	v_cvt_pk_fp8_f32 v249, v241, v245 op_sel:[0,0,1]
	v_mul_f32_e32 v234, 0x42000000, v234
	v_mul_f32_e32 v238, 0x42000000, v238
	v_mul_f32_e32 v242, 0x42000000, v242
	v_mul_f32_e32 v246, 0x42000000, v246
	v_mov_b32_e32 v250, 0
	v_cvt_pk_fp8_f32 v250, v234, v238
	v_cvt_pk_fp8_f32 v250, v242, v246 op_sel:[0,0,1]
	v_mul_f32_e32 v235, 0x42000000, v235
	v_mul_f32_e32 v239, 0x42000000, v239
	v_mul_f32_e32 v243, 0x42000000, v243
	v_mul_f32_e32 v247, 0x42000000, v247
	v_mov_b32_e32 v251, 0
	v_cvt_pk_fp8_f32 v251, v235, v239
	v_cvt_pk_fp8_f32 v251, v243, v247 op_sel:[0,0,1]
	v_mbcnt_lo_u32_b32 v253, -1, 0
	v_mbcnt_hi_u32_b32 v253, -1, v253
	v_lshlrev_b32_e32 v252, 6, v253
	s_and_b32 s100, s98, 7
	s_lshl_b32 s100, s100, 12
	s_add_i32 s100, s100, 0x11000
	s_and_b32 s101, s99, 3
	s_lshl_b32 s101, s101, 2
	s_add_i32 s100, s100, s101
	v_add_u32_e32 v252, s100, v252
	ds_write_b32 v252, v248
	ds_write_b32 v252, v249 offset:16
	ds_write_b32 v252, v250 offset:32
	ds_write_b32 v252, v251 offset:48
	s_cmp_eq_u32 s101, 12
	s_cbranch_scc0 .Latt_cv_nostore
	v_add_u32_e32 v252, -12, v252
	s_waitcnt lgkmcnt(0)
	ds_read_b128 v[232:235], v252
	ds_read_b128 v[236:239], v252 offset:16
	ds_read_b128 v[240:243], v252 offset:32
	ds_read_b128 v[244:247], v252 offset:48
	s_lshr_b32 s100, s99, 2
	s_add_i32 s100, s100, 32
	s_lshl_b32 s100, s100, 11
	s_and_b32 s101, s98, 0x7ff
	s_add_i32 s100, s100, s101
	s_sub_i32 s101, s100, 0x10000
	s_lshr_b32 s101, s101, 10
	s_lshl_b32 s101, s101, 22
	v_mov_b32_e32 v248, s101
	s_and_b32 s101, s100, 63
	s_lshl_b32 s101, s101, 16
	v_add_u32_e32 v248, s101, v248
	s_bfe_u32 s101, s100, 0x40006
	s_lshl_b32 s101, s101, 7
	v_add_u32_e32 v248, s101, v248
	v_lshrrev_b32_e32 v249, 3, v253
	v_and_b32_e32 v250, 7, v253
	v_lshl_add_u32 v248, v249, 4, v248
	v_lshl_add_u32 v248, v250, 13, v248
	v_readlane_b32 s100, v254, 48
	v_readlane_b32 s101, v254, 49
	s_add_u32 s100, s100, 0x14d59400
	s_addc_u32 s101, s101, 0
	s_waitcnt lgkmcnt(0)
	global_store_dwordx4 v248, v[232:235], s[100:101] nt
	global_store_dwordx4 v248, v[236:239], s[100:101] offset:2048 nt
	v_add_u32_e32 v249, 0x1000, v248
	global_store_dwordx4 v249, v[240:243], s[100:101] nt
	global_store_dwordx4 v249, v[244:247], s[100:101] offset:2048 nt

; __device__ __forceinline__ float sigmoidf_(float x) { return __builtin_amdgcn_rcpf(1.f + __expf(-x)); }
;     __device__ __forceinline__ void operator()(const g8::Acc& acc, const g8::Unit& u, int wr, int wc, int fr, int fq) const {
;         const int row0 = u.pm * 256 + wr * 64 + fr, j0 = u.pn * 128 + wc * 32 + 8 * fq;
;         const float* bg = bgu + (size_t)u.e * 4096 + j0; const float* bu = bg + 2048;
;         const f32x4 g0 = *(const f32x4*)bg, g1 = *(const f32x4*)(bg + 4), u0 = *(const f32x4*)bu, u1 = *(const f32x4*)(bu + 4);
; #pragma unroll
;         for (int ai = 0; ai < 2; ++ai) {
;             if (u.hm <= ai * 128 + wr * 64) break;
; #pragma unroll
;             for (int m = 0; m < 4; ++m) {
;                 f32x4 ga = acc[ai][0][m][0] * WINV + g0, gb = acc[ai][0][m][1] * WINV + g1, ua = acc[ai][1][m][0] * WINV + u0, ub = acc[ai][1][m][1] * WINV + u1;
;                 f32x4 ha, hb;
; #pragma unroll
;                 for (int j = 0; j < 4; ++j) {
;                     const float gt = fminf(ga[j], 7.f), up = fminf(fmaxf(ua[j], -7.f), 7.f);
;                     ha[j] = (up + 1.f) * gt * sigmoidf_(1.702f * gt);
;                     const float gt2 = fminf(gb[j], 7.f), up2 = fminf(fmaxf(ub[j], -7.f), 7.f);
;                     hb[j] = (up2 + 1.f) * gt2 * sigmoidf_(1.702f * gt2);
;                 }
;                 u32x2 w; w.x = pk4_fp8s(ha[0], ha[1], ha[2], ha[3]); w.y = pk4_fp8s(hb[0], hb[1], hb[2], hb[3]);
;                 *(u32x2*)(HID + (size_t)(row0 + ai * 128 + m * 16) * 2048 + j0) = w;
;             }
;         }
.Lp9e_joined:
	v_fmamk_f32 v67, v193, 0x3d000000, v209
	v_fmamk_f32 v66, v184, 0x3d000000, v200
	v_min_f32_e32 v66, 0x40e00000, v66
	v_fmamk_f32 v184, v185, 0x3d000000, v201
	v_fmamk_f32 v185, v194, 0x3d000000, v210
	v_mul_f32_e32 v194, 0x3fd9db23, v66
	v_min_f32_e32 v67, 0x40e00000, v67
	v_mul_f32_e32 v194, 0xbfb8aa3b, v194
	v_fmamk_f32 v64, v192, 0x3d000000, v208
	v_fmamk_f32 v192, v195, 0x3d000000, v211
	v_mul_f32_e32 v195, 0x3fd9db23, v67
	v_exp_f32_e32 v194, v194
	v_fmamk_f32 v180, v180, 0x3d000000, v196
	v_fmamk_f32 v181, v181, 0x3d000000, v197
	v_fmamk_f32 v190, v190, 0x3d000000, v206
	v_mul_f32_e32 v195, 0xbfb8aa3b, v195
	v_med3_f32 v180, v180, s71, v235
	v_med3_f32 v181, v181, s71, v235
	v_med3_f32 v190, v190, s71, v235
	v_exp_f32_e32 v195, v195
	v_min_f32_e32 v184, 0x40e00000, v184
	v_min_f32_e32 v185, 0x40e00000, v185
	v_fmamk_f32 v182, v182, 0x3d000000, v198
	v_add_f32_e32 v180, 1.0, v180
	v_add_f32_e32 v181, 1.0, v181
	v_add_f32_e32 v190, 1.0, v190
	v_fmamk_f32 v186, v186, 0x3d000000, v202
	v_mul_f32_e32 v241, 0x3fd9db23, v185
	v_med3_f32 v182, v182, s71, v235
	v_mul_f32_e32 v66, v66, v180
	v_mul_f32_e32 v180, v184, v181
	v_mul_f32_e32 v181, v185, v190
	v_add_f32_e32 v185, 1.0, v194
	v_min_f32_e32 v64, 0x40e00000, v64
	v_min_f32_e32 v186, 0x40e00000, v186
	v_add_f32_e32 v182, 1.0, v182
	v_rcp_f32_e32 v185, v185
	v_mul_f32_e32 v193, 0x3fd9db23, v64
	v_mul_f32_e32 v223, 0x3fd9db23, v184
	v_mul_f32_e32 v242, 0x3fd9db23, v186
	v_mul_f32_e32 v182, v186, v182
	v_add_f32_e32 v186, 1.0, v195
	v_fmamk_f32 v189, v189, 0x3d000000, v205
	v_mul_f32_e32 v193, 0xbfb8aa3b, v193
	v_mul_f32_e32 v223, 0xbfb8aa3b, v223
	v_mul_f32_e32 v241, 0xbfb8aa3b, v241
	v_rcp_f32_e32 v186, v186
	v_med3_f32 v189, v189, s71, v235
	v_exp_f32_e32 v193, v193
	v_exp_f32_e32 v223, v223
	v_exp_f32_e32 v241, v241
	v_min_f32_e32 v192, 0x40e00000, v192
	v_fmamk_f32 v188, v188, 0x3d000000, v204
	v_add_f32_e32 v189, 1.0, v189
	v_mul_f32_e32 v66, v66, v185
	v_fmamk_f32 v185, v187, 0x3d000000, v203
	v_mul_f32_e32 v243, 0x3fd9db23, v192
	v_med3_f32 v188, v188, s71, v235
	v_mul_f32_e32 v67, v67, v189
	v_min_f32_e32 v185, 0x40e00000, v185
	v_mul_f32_e32 v243, 0xbfb8aa3b, v243
	v_add_f32_e32 v188, 1.0, v188
	v_mul_f32_e32 v67, v67, v186
	v_mul_f32_e32 v186, 0x3fd9db23, v185
	v_exp_f32_e32 v243, v243
	v_mul_f32_e32 v64, v64, v188
	v_add_f32_e32 v184, 1.0, v193
	v_add_f32_e32 v188, 1.0, v223
	v_add_f32_e32 v189, 1.0, v241
	v_mul_f32_e32 v186, 0xbfb8aa3b, v186
	v_rcp_f32_e32 v184, v184
	v_rcp_f32_e32 v188, v188
	v_rcp_f32_e32 v189, v189
	v_exp_f32_e32 v186, v186
	v_mul_f32_e32 v242, 0xbfb8aa3b, v242
	v_exp_f32_e32 v242, v242
	v_add_f32_e32 v193, 1.0, v243
	v_fmamk_f32 v191, v191, 0x3d000000, v207
	v_mul_f32_e32 v64, v64, v184
	v_mul_f32_e32 v184, v180, v188
	v_mul_f32_e32 v180, v181, v189
	v_rcp_f32_e32 v181, v193
	v_add_f32_e32 v186, 1.0, v186
	v_med3_f32 v191, v191, s71, v235
	v_fmamk_f32 v183, v183, 0x3d000000, v199
	v_rcp_f32_e32 v186, v186
	v_add_f32_e32 v191, 1.0, v191
	v_med3_f32 v183, v183, s71, v235
	v_add_f32_e32 v190, 1.0, v242
	v_mul_f32_e32 v187, v192, v191
	v_add_f32_e32 v183, 1.0, v183
	v_rcp_f32_e32 v190, v190
	v_mul_f32_e32 v181, v187, v181
	v_mul_f32_e32 v183, v185, v183
	v_med3_f32 v64, v64, s72, v236
	v_med3_f32 v67, v67, s72, v236
	v_med3_f32 v185, v180, s72, v236
	v_mov_b32_e32 v180, v65
	v_mul_f32_e32 v183, v183, v186
	v_med3_f32 v186, v181, s72, v236
	v_cvt_pk_fp8_f32 v180, v64, v67
	v_med3_f32 v64, v66, s72, v236
	v_med3_f32 v66, v184, s72, v236
	v_mov_b32_e32 v181, v65
	v_cvt_pk_fp8_f32 v181, v64, v66
	v_mul_f32_e32 v182, v182, v190
	v_med3_f32 v64, v182, s72, v236
	v_med3_f32 v66, v183, s72, v236
	v_cvt_pk_fp8_f32 v180, v185, v186 op_sel:[0,0,1]
	v_cvt_pk_fp8_f32 v181, v64, v66 op_sel:[0,0,1]
	v_ashrrev_i32_e32 v223, 31, v222
	v_lshlrev_b64 v[66:67], 11, v[222:223]
	v_lshl_add_u64 v[66:67], s[16:17], 0, v[66:67]
	v_fmamk_f32 v64, v176, 0x3d000000, v208
	v_fmamk_f32 v172, v172, 0x3d000000, v200
	v_lshl_add_u64 v[66:67], v[66:67], 0, v[220:221]
	v_min_f32_e32 v64, 0x40e00000, v64
	v_min_f32_e32 v172, 0x40e00000, v172
	global_store_dwordx2 v[66:67], v[180:181], off
	v_mul_f32_e32 v176, 0x3fd9db23, v64
	v_mul_f32_e32 v180, 0x3fd9db23, v172
	v_mul_f32_e32 v176, 0xbfb8aa3b, v176
	v_mul_f32_e32 v180, 0xbfb8aa3b, v180
	v_exp_f32_e32 v176, v176
	v_exp_f32_e32 v180, v180
	v_fmamk_f32 v168, v168, 0x3d000000, v204
	v_med3_f32 v168, v168, s71, v235
	v_add_f32_e32 v168, 1.0, v168
	v_add_f32_e32 v176, 1.0, v176
	v_mul_f32_e32 v64, v64, v168
	v_add_f32_e32 v168, 1.0, v180
	v_rcp_f32_e32 v176, v176
	v_fmamk_f32 v164, v164, 0x3d000000, v196
	v_rcp_f32_e32 v168, v168
	v_med3_f32 v164, v164, s71, v235
	v_add_f32_e32 v164, 1.0, v164
	v_fmamk_f32 v173, v173, 0x3d000000, v201
	v_mul_f32_e32 v164, v172, v164
	v_min_f32_e32 v173, 0x40e00000, v173
	v_mul_f32_e32 v64, v64, v176
	v_mul_f32_e32 v168, v164, v168
	v_fmamk_f32 v164, v177, 0x3d000000, v209
	v_mul_f32_e32 v176, 0x3fd9db23, v173
	v_min_f32_e32 v164, 0x40e00000, v164
	v_mul_f32_e32 v176, 0xbfb8aa3b, v176
	v_mul_f32_e32 v172, 0x3fd9db23, v164
	v_exp_f32_e32 v176, v176
	v_mul_f32_e32 v172, 0xbfb8aa3b, v172
	v_fmamk_f32 v169, v169, 0x3d000000, v205
	v_exp_f32_e32 v172, v172
	v_med3_f32 v169, v169, s71, v235
	v_add_f32_e32 v169, 1.0, v169
	v_mul_f32_e32 v164, v164, v169
	v_fmamk_f32 v165, v165, 0x3d000000, v197
	v_add_f32_e32 v169, 1.0, v176
	v_rcp_f32_e32 v169, v169
	v_med3_f32 v165, v165, s71, v235
	v_add_f32_e32 v172, 1.0, v172
	v_add_f32_e32 v165, 1.0, v165
	v_rcp_f32_e32 v172, v172
	v_mul_f32_e32 v165, v173, v165
	v_fmamk_f32 v173, v174, 0x3d000000, v202
	v_min_f32_e32 v173, 0x40e00000, v173
	v_mul_f32_e32 v165, v165, v169
; __device__ __forceinline__ float sigmoidf_(float x) { return __builtin_amdgcn_rcpf(1.f + __expf(-x)); }
;     __device__ __forceinline__ void operator()(const g8::Acc& acc, const g8::Unit& u, int wr, int wc, int fr, int fq) const {
;         const int row0 = u.pm * 256 + wr * 64 + fr, j0 = u.pn * 128 + wc * 32 + 8 * fq;
;         const float* bg = bgu + (size_t)u.e * 4096 + j0; const float* bu = bg + 2048;
;         const f32x4 g0 = *(const f32x4*)bg, g1 = *(const f32x4*)(bg + 4), u0 = *(const f32x4*)bu, u1 = *(const f32x4*)(bu + 4);
; #pragma unroll
;         for (int ai = 0; ai < 2; ++ai) {
;             if (u.hm <= ai * 128 + wr * 64) break;
; #pragma unroll
;             for (int m = 0; m < 4; ++m) {
;                 f32x4 ga = acc[ai][0][m][0] * WINV + g0, gb = acc[ai][0][m][1] * WINV + g1, ua = acc[ai][1][m][0] * WINV + u0, ub = acc[ai][1][m][1] * WINV + u1;
;                 f32x4 ha, hb;
; #pragma unroll
;                 for (int j = 0; j < 4; ++j) {
;                     const float gt = fminf(ga[j], 7.f), up = fminf(fmaxf(ua[j], -7.f), 7.f);
;                     ha[j] = (up + 1.f) * gt * sigmoidf_(1.702f * gt);
;                     const float gt2 = fminf(gb[j], 7.f), up2 = fminf(fmaxf(ub[j], -7.f), 7.f);
;                     hb[j] = (up2 + 1.f) * gt2 * sigmoidf_(1.702f * gt2);
;                 }
;                 u32x2 w; w.x = pk4_fp8s(ha[0], ha[1], ha[2], ha[3]); w.y = pk4_fp8s(hb[0], hb[1], hb[2], hb[3]);
;                 *(u32x2*)(HID + (size_t)(row0 + ai * 128 + m * 16) * 2048 + j0) = w;
;             }
;         }
	v_fmamk_f32 v169, v178, 0x3d000000, v210
	v_mul_f32_e32 v174, 0x3fd9db23, v173
	v_min_f32_e32 v169, 0x40e00000, v169
	v_mul_f32_e32 v174, 0xbfb8aa3b, v174
	v_mul_f32_e32 v164, v164, v172
	v_mul_f32_e32 v172, 0x3fd9db23, v169
	v_exp_f32_e32 v174, v174
	v_mul_f32_e32 v172, 0xbfb8aa3b, v172
	v_fmamk_f32 v170, v170, 0x3d000000, v206
	v_fmamk_f32 v166, v166, 0x3d000000, v198
	v_exp_f32_e32 v172, v172
	v_med3_f32 v170, v170, s71, v235
	v_med3_f32 v166, v166, s71, v235
	v_add_f32_e32 v170, 1.0, v170
	v_add_f32_e32 v166, 1.0, v166
	v_mul_f32_e32 v169, v169, v170
	v_add_f32_e32 v170, 1.0, v174
	v_mul_f32_e32 v166, v173, v166
	v_fmamk_f32 v173, v175, 0x3d000000, v203
	v_rcp_f32_e32 v170, v170
	v_min_f32_e32 v173, 0x40e00000, v173
	v_add_f32_e32 v172, 1.0, v172
	v_mul_f32_e32 v174, 0x3fd9db23, v173
	v_rcp_f32_e32 v172, v172
	v_mul_f32_e32 v174, 0xbfb8aa3b, v174
	v_exp_f32_e32 v174, v174
	v_mul_f32_e32 v166, v166, v170
	v_fmamk_f32 v170, v179, 0x3d000000, v211
	v_fmamk_f32 v171, v171, 0x3d000000, v207
	v_min_f32_e32 v170, 0x40e00000, v170
	v_med3_f32 v171, v171, s71, v235
	v_mul_f32_e32 v169, v169, v172
	v_mul_f32_e32 v172, 0x3fd9db23, v170
	v_add_f32_e32 v171, 1.0, v171
	v_mul_f32_e32 v172, 0xbfb8aa3b, v172
	v_mul_f32_e32 v170, v170, v171
	v_add_f32_e32 v171, 1.0, v174
	v_exp_f32_e32 v172, v172
	v_fmamk_f32 v167, v167, 0x3d000000, v199
	v_rcp_f32_e32 v171, v171
	v_med3_f32 v167, v167, s71, v235
	v_add_f32_e32 v167, 1.0, v167
	v_mul_f32_e32 v167, v173, v167
	v_add_f32_e32 v172, 1.0, v172
	v_mul_f32_e32 v167, v167, v171
	v_med3_f32 v64, v64, s72, v236
	v_med3_f32 v171, v164, s72, v236
	v_mov_b32_e32 v164, v65
	v_rcp_f32_e32 v172, v172
	v_cvt_pk_fp8_f32 v164, v64, v171
	v_med3_f32 v64, v168, s72, v236
	v_med3_f32 v168, v165, s72, v236
	v_mov_b32_e32 v165, v65
	v_cvt_pk_fp8_f32 v165, v64, v168
	v_mul_f32_e32 v170, v170, v172
	v_med3_f32 v64, v166, s72, v236
	v_med3_f32 v166, v167, s72, v236
	v_med3_f32 v169, v169, s72, v236
	v_med3_f32 v170, v170, s72, v236
	v_cvt_pk_fp8_f32 v165, v64, v166 op_sel:[0,0,1]
	v_or_b32_e32 v166, 16, v222
	v_cvt_pk_fp8_f32 v164, v169, v170 op_sel:[0,0,1]
	v_ashrrev_i32_e32 v167, 31, v166
	v_lshlrev_b64 v[166:167], 11, v[166:167]
	v_lshl_add_u64 v[166:167], s[16:17], 0, v[166:167]
	v_fmamk_f32 v64, v160, 0x3d000000, v208
	v_fmamk_f32 v156, v156, 0x3d000000, v200
	v_lshl_add_u64 v[166:167], v[166:167], 0, v[220:221]
	v_min_f32_e32 v64, 0x40e00000, v64
	v_min_f32_e32 v156, 0x40e00000, v156
	global_store_dwordx2 v[166:167], v[164:165], off
	v_mul_f32_e32 v160, 0x3fd9db23, v64
	v_mul_f32_e32 v164, 0x3fd9db23, v156
	v_mul_f32_e32 v160, 0xbfb8aa3b, v160
	v_mul_f32_e32 v164, 0xbfb8aa3b, v164
	v_exp_f32_e32 v160, v160
	v_exp_f32_e32 v164, v164
	v_fmamk_f32 v152, v152, 0x3d000000, v204
	v_med3_f32 v152, v152, s71, v235
	v_add_f32_e32 v152, 1.0, v152
	v_add_f32_e32 v160, 1.0, v160
	v_mul_f32_e32 v64, v64, v152
	v_add_f32_e32 v152, 1.0, v164
	v_rcp_f32_e32 v160, v160
	v_fmamk_f32 v148, v148, 0x3d000000, v196
	v_rcp_f32_e32 v152, v152
	v_med3_f32 v148, v148, s71, v235
	v_add_f32_e32 v148, 1.0, v148
	v_fmamk_f32 v157, v157, 0x3d000000, v201
	v_mul_f32_e32 v148, v156, v148
	v_min_f32_e32 v157, 0x40e00000, v157
	v_mul_f32_e32 v64, v64, v160
	v_mul_f32_e32 v152, v148, v152
	v_fmamk_f32 v148, v161, 0x3d000000, v209
	v_mul_f32_e32 v160, 0x3fd9db23, v157
	v_min_f32_e32 v148, 0x40e00000, v148
	v_mul_f32_e32 v160, 0xbfb8aa3b, v160
	v_mul_f32_e32 v156, 0x3fd9db23, v148
	v_exp_f32_e32 v160, v160
	v_mul_f32_e32 v156, 0xbfb8aa3b, v156
	v_fmamk_f32 v153, v153, 0x3d000000, v205
	v_exp_f32_e32 v156, v156
	v_med3_f32 v153, v153, s71, v235
	v_add_f32_e32 v153, 1.0, v153
	v_mul_f32_e32 v148, v148, v153
	v_fmamk_f32 v149, v149, 0x3d000000, v197
	v_add_f32_e32 v153, 1.0, v160
	v_rcp_f32_e32 v153, v153
	v_med3_f32 v149, v149, s71, v235
	v_add_f32_e32 v156, 1.0, v156
	v_add_f32_e32 v149, 1.0, v149
	v_rcp_f32_e32 v156, v156
	v_mul_f32_e32 v149, v157, v149
	v_fmamk_f32 v157, v158, 0x3d000000, v202
	v_min_f32_e32 v157, 0x40e00000, v157
	v_mul_f32_e32 v149, v149, v153
	v_fmamk_f32 v153, v162, 0x3d000000, v210
	v_mul_f32_e32 v158, 0x3fd9db23, v157
	v_min_f32_e32 v153, 0x40e00000, v153
	v_mul_f32_e32 v158, 0xbfb8aa3b, v158
	v_mul_f32_e32 v148, v148, v156
	v_mul_f32_e32 v156, 0x3fd9db23, v153
	v_exp_f32_e32 v158, v158
	v_mul_f32_e32 v156, 0xbfb8aa3b, v156
	v_fmamk_f32 v154, v154, 0x3d000000, v206
	v_fmamk_f32 v150, v150, 0x3d000000, v198
	v_exp_f32_e32 v156, v156
	v_med3_f32 v154, v154, s71, v235
	v_med3_f32 v150, v150, s71, v235
	v_add_f32_e32 v154, 1.0, v154
	v_add_f32_e32 v150, 1.0, v150
	v_mul_f32_e32 v153, v153, v154
	v_add_f32_e32 v154, 1.0, v158
	v_mul_f32_e32 v150, v157, v150
	v_fmamk_f32 v157, v159, 0x3d000000, v203
	v_rcp_f32_e32 v154, v154
	v_min_f32_e32 v157, 0x40e00000, v157
	v_add_f32_e32 v156, 1.0, v156
	v_mul_f32_e32 v158, 0x3fd9db23, v157
	v_rcp_f32_e32 v156, v156
	v_mul_f32_e32 v158, 0xbfb8aa3b, v158
	v_exp_f32_e32 v158, v158
	v_mul_f32_e32 v150, v150, v154
	v_fmamk_f32 v154, v163, 0x3d000000, v211
	v_fmamk_f32 v155, v155, 0x3d000000, v207
	v_min_f32_e32 v154, 0x40e00000, v154
	v_med3_f32 v155, v155, s71, v235
	v_mul_f32_e32 v153, v153, v156
	v_mul_f32_e32 v156, 0x3fd9db23, v154
	v_add_f32_e32 v155, 1.0, v155
	v_mul_f32_e32 v156, 0xbfb8aa3b, v156
	v_mul_f32_e32 v154, v154, v155
	v_add_f32_e32 v155, 1.0, v158
	v_exp_f32_e32 v156, v156
	v_fmamk_f32 v151, v151, 0x3d000000, v199
	v_rcp_f32_e32 v155, v155
	v_med3_f32 v151, v151, s71, v235
	v_add_f32_e32 v151, 1.0, v151
	v_mul_f32_e32 v151, v157, v151
	v_add_f32_e32 v156, 1.0, v156
	v_mul_f32_e32 v151, v151, v155
	v_med3_f32 v64, v64, s72, v236
	v_med3_f32 v155, v148, s72, v236
	v_mov_b32_e32 v148, v65
; __device__ __forceinline__ float sigmoidf_(float x) { return __builtin_amdgcn_rcpf(1.f + __expf(-x)); }
;     __device__ __forceinline__ void operator()(const g8::Acc& acc, const g8::Unit& u, int wr, int wc, int fr, int fq) const {
;         const int row0 = u.pm * 256 + wr * 64 + fr, j0 = u.pn * 128 + wc * 32 + 8 * fq;
;         const float* bg = bgu + (size_t)u.e * 4096 + j0; const float* bu = bg + 2048;
;         const f32x4 g0 = *(const f32x4*)bg, g1 = *(const f32x4*)(bg + 4), u0 = *(const f32x4*)bu, u1 = *(const f32x4*)(bu + 4);
; #pragma unroll
;         for (int ai = 0; ai < 2; ++ai) {
;             if (u.hm <= ai * 128 + wr * 64) break;
; #pragma unroll
;             for (int m = 0; m < 4; ++m) {
;                 f32x4 ga = acc[ai][0][m][0] * WINV + g0, gb = acc[ai][0][m][1] * WINV + g1, ua = acc[ai][1][m][0] * WINV + u0, ub = acc[ai][1][m][1] * WINV + u1;
;                 f32x4 ha, hb;
; #pragma unroll
;                 for (int j = 0; j < 4; ++j) {
;                     const float gt = fminf(ga[j], 7.f), up = fminf(fmaxf(ua[j], -7.f), 7.f);
;                     ha[j] = (up + 1.f) * gt * sigmoidf_(1.702f * gt);
;                     const float gt2 = fminf(gb[j], 7.f), up2 = fminf(fmaxf(ub[j], -7.f), 7.f);
;                     hb[j] = (up2 + 1.f) * gt2 * sigmoidf_(1.702f * gt2);
;                 }
;                 u32x2 w; w.x = pk4_fp8s(ha[0], ha[1], ha[2], ha[3]); w.y = pk4_fp8s(hb[0], hb[1], hb[2], hb[3]);
;                 *(u32x2*)(HID + (size_t)(row0 + ai * 128 + m * 16) * 2048 + j0) = w;
;             }
;         }
	v_rcp_f32_e32 v156, v156
	v_cvt_pk_fp8_f32 v148, v64, v155
	v_med3_f32 v64, v152, s72, v236
	v_med3_f32 v152, v149, s72, v236
	v_mov_b32_e32 v149, v65
	v_cvt_pk_fp8_f32 v149, v64, v152
	v_mul_f32_e32 v154, v154, v156
	v_med3_f32 v64, v150, s72, v236
	v_med3_f32 v150, v151, s72, v236
	v_med3_f32 v153, v153, s72, v236
	v_med3_f32 v154, v154, s72, v236
	v_cvt_pk_fp8_f32 v149, v64, v150 op_sel:[0,0,1]
	v_or_b32_e32 v150, 32, v222
	v_cvt_pk_fp8_f32 v148, v153, v154 op_sel:[0,0,1]
	v_ashrrev_i32_e32 v151, 31, v150
	v_lshlrev_b64 v[150:151], 11, v[150:151]
	v_lshl_add_u64 v[150:151], s[16:17], 0, v[150:151]
	v_fmamk_f32 v64, v144, 0x3d000000, v208
	v_fmamk_f32 v140, v140, 0x3d000000, v200
	v_lshl_add_u64 v[150:151], v[150:151], 0, v[220:221]
	v_min_f32_e32 v64, 0x40e00000, v64
	v_min_f32_e32 v140, 0x40e00000, v140
	global_store_dwordx2 v[150:151], v[148:149], off
	v_mul_f32_e32 v144, 0x3fd9db23, v64
	v_mul_f32_e32 v148, 0x3fd9db23, v140
	v_mul_f32_e32 v144, 0xbfb8aa3b, v144
	v_mul_f32_e32 v148, 0xbfb8aa3b, v148
	v_exp_f32_e32 v144, v144
	v_exp_f32_e32 v148, v148
	v_fmamk_f32 v136, v136, 0x3d000000, v204
	v_med3_f32 v136, v136, s71, v235
	v_add_f32_e32 v136, 1.0, v136
	v_add_f32_e32 v144, 1.0, v144
	v_mul_f32_e32 v64, v64, v136
	v_add_f32_e32 v136, 1.0, v148
	v_rcp_f32_e32 v144, v144
	v_fmamk_f32 v132, v132, 0x3d000000, v196
	v_rcp_f32_e32 v136, v136
	v_med3_f32 v132, v132, s71, v235
	v_add_f32_e32 v132, 1.0, v132
	v_fmamk_f32 v141, v141, 0x3d000000, v201
	v_mul_f32_e32 v132, v140, v132
	v_min_f32_e32 v141, 0x40e00000, v141
	v_mul_f32_e32 v64, v64, v144
	v_mul_f32_e32 v136, v132, v136
	v_fmamk_f32 v132, v145, 0x3d000000, v209
	v_mul_f32_e32 v144, 0x3fd9db23, v141
	v_min_f32_e32 v132, 0x40e00000, v132
	v_mul_f32_e32 v144, 0xbfb8aa3b, v144
	v_mul_f32_e32 v140, 0x3fd9db23, v132
	v_exp_f32_e32 v144, v144
	v_mul_f32_e32 v140, 0xbfb8aa3b, v140
	v_fmamk_f32 v137, v137, 0x3d000000, v205
	v_exp_f32_e32 v140, v140
	v_med3_f32 v137, v137, s71, v235
	v_add_f32_e32 v137, 1.0, v137
	v_mul_f32_e32 v132, v132, v137
	v_fmamk_f32 v133, v133, 0x3d000000, v197
	v_add_f32_e32 v137, 1.0, v144
	v_rcp_f32_e32 v137, v137
	v_med3_f32 v133, v133, s71, v235
	v_add_f32_e32 v140, 1.0, v140
	v_add_f32_e32 v133, 1.0, v133
	v_rcp_f32_e32 v140, v140
	v_mul_f32_e32 v133, v141, v133
	v_fmamk_f32 v141, v142, 0x3d000000, v202
	v_min_f32_e32 v141, 0x40e00000, v141
	v_mul_f32_e32 v133, v133, v137
	v_fmamk_f32 v137, v146, 0x3d000000, v210
	v_mul_f32_e32 v142, 0x3fd9db23, v141
	v_min_f32_e32 v137, 0x40e00000, v137
	v_mul_f32_e32 v142, 0xbfb8aa3b, v142
	v_mul_f32_e32 v132, v132, v140
	v_mul_f32_e32 v140, 0x3fd9db23, v137
	v_exp_f32_e32 v142, v142
	v_mul_f32_e32 v140, 0xbfb8aa3b, v140
	v_fmamk_f32 v138, v138, 0x3d000000, v206
	v_fmamk_f32 v134, v134, 0x3d000000, v198
	v_exp_f32_e32 v140, v140
	v_med3_f32 v138, v138, s71, v235
	v_med3_f32 v134, v134, s71, v235
	v_add_f32_e32 v138, 1.0, v138
	v_add_f32_e32 v134, 1.0, v134
	v_mul_f32_e32 v137, v137, v138
	v_add_f32_e32 v138, 1.0, v142
	v_mul_f32_e32 v134, v141, v134
	v_fmamk_f32 v141, v143, 0x3d000000, v203
	v_rcp_f32_e32 v138, v138
	v_min_f32_e32 v141, 0x40e00000, v141
	v_add_f32_e32 v140, 1.0, v140
	v_mul_f32_e32 v142, 0x3fd9db23, v141
	v_rcp_f32_e32 v140, v140
	v_mul_f32_e32 v142, 0xbfb8aa3b, v142
	v_exp_f32_e32 v142, v142
	v_mul_f32_e32 v134, v134, v138
	v_fmamk_f32 v138, v147, 0x3d000000, v211
	v_fmamk_f32 v139, v139, 0x3d000000, v207
	v_min_f32_e32 v138, 0x40e00000, v138
	v_med3_f32 v139, v139, s71, v235
	v_mul_f32_e32 v137, v137, v140
	v_mul_f32_e32 v140, 0x3fd9db23, v138
	v_add_f32_e32 v139, 1.0, v139
	v_mul_f32_e32 v140, 0xbfb8aa3b, v140
	v_mul_f32_e32 v138, v138, v139
	v_add_f32_e32 v139, 1.0, v142
	v_exp_f32_e32 v140, v140
	v_fmamk_f32 v135, v135, 0x3d000000, v199
	v_rcp_f32_e32 v139, v139
	v_med3_f32 v135, v135, s71, v235
	v_add_f32_e32 v135, 1.0, v135
	v_mul_f32_e32 v135, v141, v135
	v_add_f32_e32 v140, 1.0, v140
	v_mul_f32_e32 v135, v135, v139
	v_med3_f32 v64, v64, s72, v236
	v_med3_f32 v139, v132, s72, v236
	v_mov_b32_e32 v132, v65
	v_rcp_f32_e32 v140, v140
	v_cvt_pk_fp8_f32 v132, v64, v139
	v_med3_f32 v64, v136, s72, v236
	v_med3_f32 v136, v133, s72, v236
	v_mov_b32_e32 v133, v65
	v_cvt_pk_fp8_f32 v133, v64, v136
	v_mul_f32_e32 v138, v138, v140
	v_med3_f32 v64, v134, s72, v236
	v_med3_f32 v134, v135, s72, v236
	v_med3_f32 v137, v137, s72, v236
	v_med3_f32 v138, v138, s72, v236
	v_cvt_pk_fp8_f32 v133, v64, v134 op_sel:[0,0,1]
	v_or_b32_e32 v134, 48, v222
	v_cvt_pk_fp8_f32 v132, v137, v138 op_sel:[0,0,1]
	v_ashrrev_i32_e32 v135, 31, v134
	v_lshlrev_b64 v[134:135], 11, v[134:135]
	v_lshl_add_u64 v[134:135], s[16:17], 0, v[134:135]
	v_lshl_add_u64 v[134:135], v[134:135], 0, v[220:221]
	global_store_dwordx2 v[134:135], v[132:133], off
	s_cbranch_vccnz .Lp9_fin4
; __device__ __forceinline__ float sigmoidf_(float x) { return __builtin_amdgcn_rcpf(1.f + __expf(-x)); }
;     __device__ __forceinline__ void operator()(const g8::Acc& acc, const g8::Unit& u, int wr, int wc, int fr, int fq) const {
;         const int row0 = u.pm * 256 + wr * 64 + fr, j0 = u.pn * 128 + wc * 32 + 8 * fq;
;         const float* bg = bgu + (size_t)u.e * 4096 + j0; const float* bu = bg + 2048;
;         const f32x4 g0 = *(const f32x4*)bg, g1 = *(const f32x4*)(bg + 4), u0 = *(const f32x4*)bu, u1 = *(const f32x4*)(bu + 4);
; #pragma unroll
;         for (int ai = 0; ai < 2; ++ai) {
;             if (u.hm <= ai * 128 + wr * 64) break;
; #pragma unroll
;             for (int m = 0; m < 4; ++m) {
;                 f32x4 ga = acc[ai][0][m][0] * WINV + g0, gb = acc[ai][0][m][1] * WINV + g1, ua = acc[ai][1][m][0] * WINV + u0, ub = acc[ai][1][m][1] * WINV + u1;
;                 f32x4 ha, hb;
; #pragma unroll
;                 for (int j = 0; j < 4; ++j) {
;                     const float gt = fminf(ga[j], 7.f), up = fminf(fmaxf(ua[j], -7.f), 7.f);
;                     ha[j] = (up + 1.f) * gt * sigmoidf_(1.702f * gt);
;                     const float gt2 = fminf(gb[j], 7.f), up2 = fminf(fmaxf(ub[j], -7.f), 7.f);
;                     hb[j] = (up2 + 1.f) * gt2 * sigmoidf_(1.702f * gt2);
;                 }
;                 u32x2 w; w.x = pk4_fp8s(ha[0], ha[1], ha[2], ha[3]); w.y = pk4_fp8s(hb[0], hb[1], hb[2], hb[3]);
;                 *(u32x2*)(HID + (size_t)(row0 + ai * 128 + m * 16) * 2048 + j0) = w;
;             }
;         }
	v_fmamk_f32 v64, v128, 0x3d000000, v208
	v_fmamk_f32 v124, v124, 0x3d000000, v200
	v_min_f32_e32 v64, 0x40e00000, v64
	v_min_f32_e32 v124, 0x40e00000, v124
	v_mul_f32_e32 v128, 0x3fd9db23, v64
	v_mul_f32_e32 v132, 0x3fd9db23, v124
	v_mul_f32_e32 v128, 0xbfb8aa3b, v128
	v_mul_f32_e32 v132, 0xbfb8aa3b, v132
	v_exp_f32_e32 v128, v128
	v_exp_f32_e32 v132, v132
	v_fmamk_f32 v120, v120, 0x3d000000, v204
	v_med3_f32 v120, v120, s71, v235
	v_add_f32_e32 v120, 1.0, v120
	v_add_f32_e32 v128, 1.0, v128
	v_mul_f32_e32 v64, v64, v120
	v_add_f32_e32 v120, 1.0, v132
	v_rcp_f32_e32 v128, v128
	v_fmamk_f32 v116, v116, 0x3d000000, v196
	v_rcp_f32_e32 v120, v120
	v_med3_f32 v116, v116, s71, v235
	v_add_f32_e32 v116, 1.0, v116
	v_fmamk_f32 v125, v125, 0x3d000000, v201
	v_mul_f32_e32 v116, v124, v116
	v_min_f32_e32 v125, 0x40e00000, v125
	v_mul_f32_e32 v64, v64, v128
	v_mul_f32_e32 v120, v116, v120
	v_fmamk_f32 v116, v129, 0x3d000000, v209
	v_mul_f32_e32 v128, 0x3fd9db23, v125
	v_min_f32_e32 v116, 0x40e00000, v116
	v_mul_f32_e32 v128, 0xbfb8aa3b, v128
	v_mul_f32_e32 v124, 0x3fd9db23, v116
	v_exp_f32_e32 v128, v128
	v_mul_f32_e32 v124, 0xbfb8aa3b, v124
	v_fmamk_f32 v121, v121, 0x3d000000, v205
	v_exp_f32_e32 v124, v124
	v_med3_f32 v121, v121, s71, v235
	v_add_f32_e32 v121, 1.0, v121
	v_mul_f32_e32 v116, v116, v121
	v_fmamk_f32 v117, v117, 0x3d000000, v197
	v_add_f32_e32 v121, 1.0, v128
	v_rcp_f32_e32 v121, v121
	v_med3_f32 v117, v117, s71, v235
	v_add_f32_e32 v124, 1.0, v124
	v_add_f32_e32 v117, 1.0, v117
	v_rcp_f32_e32 v124, v124
	v_mul_f32_e32 v117, v125, v117
	v_fmamk_f32 v125, v126, 0x3d000000, v202
	v_min_f32_e32 v125, 0x40e00000, v125
	v_mul_f32_e32 v117, v117, v121
	v_fmamk_f32 v121, v130, 0x3d000000, v210
	v_mul_f32_e32 v126, 0x3fd9db23, v125
	v_min_f32_e32 v121, 0x40e00000, v121
	v_mul_f32_e32 v126, 0xbfb8aa3b, v126
	v_mul_f32_e32 v116, v116, v124
	v_mul_f32_e32 v124, 0x3fd9db23, v121
	v_exp_f32_e32 v126, v126
	v_mul_f32_e32 v124, 0xbfb8aa3b, v124
	v_fmamk_f32 v122, v122, 0x3d000000, v206
	v_exp_f32_e32 v124, v124
	v_med3_f32 v122, v122, s71, v235
	v_fmamk_f32 v118, v118, 0x3d000000, v198
	v_add_f32_e32 v122, 1.0, v122
	v_med3_f32 v118, v118, s71, v235
	v_mul_f32_e32 v121, v121, v122
	v_add_f32_e32 v122, 1.0, v126
	v_add_f32_e32 v118, 1.0, v118
	v_rcp_f32_e32 v122, v122
	v_mul_f32_e32 v118, v125, v118
	v_fmamk_f32 v125, v127, 0x3d000000, v203
	v_add_f32_e32 v124, 1.0, v124
	v_min_f32_e32 v125, 0x40e00000, v125
	v_rcp_f32_e32 v124, v124
	v_mul_f32_e32 v126, 0x3fd9db23, v125
	v_mul_f32_e32 v126, 0xbfb8aa3b, v126
	v_mul_f32_e32 v118, v118, v122
	v_fmamk_f32 v122, v131, 0x3d000000, v211
	v_exp_f32_e32 v126, v126
	v_min_f32_e32 v122, 0x40e00000, v122
	v_fmamk_f32 v123, v123, 0x3d000000, v207
	v_mul_f32_e32 v121, v121, v124
	v_mul_f32_e32 v124, 0x3fd9db23, v122
	v_med3_f32 v123, v123, s71, v235
	v_mul_f32_e32 v124, 0xbfb8aa3b, v124
	v_add_f32_e32 v123, 1.0, v123
	v_exp_f32_e32 v124, v124
	v_mul_f32_e32 v122, v122, v123
	v_add_f32_e32 v123, 1.0, v126
	v_fmamk_f32 v119, v119, 0x3d000000, v199
	v_rcp_f32_e32 v123, v123
	v_med3_f32 v119, v119, s71, v235
	v_add_f32_e32 v119, 1.0, v119
	v_add_f32_e32 v124, 1.0, v124
	v_mul_f32_e32 v119, v125, v119
	v_rcp_f32_e32 v124, v124
	v_mul_f32_e32 v119, v119, v123
	v_med3_f32 v64, v64, s72, v236
	v_med3_f32 v123, v116, s72, v236
	v_mov_b32_e32 v116, v65
	v_cvt_pk_fp8_f32 v116, v64, v123
	v_med3_f32 v64, v120, s72, v236
	v_med3_f32 v120, v117, s72, v236
	v_mov_b32_e32 v117, v65
	v_cvt_pk_fp8_f32 v117, v64, v120
	v_mul_f32_e32 v122, v122, v124
	v_med3_f32 v121, v121, s72, v236
	v_med3_f32 v122, v122, s72, v236
	v_med3_f32 v64, v118, s72, v236
	v_med3_f32 v118, v119, s72, v236
	v_cvt_pk_fp8_f32 v116, v121, v122 op_sel:[0,0,1]
	v_cvt_pk_fp8_f32 v117, v64, v118 op_sel:[0,0,1]
	v_add_co_u32_e32 v118, vcc, s47, v66
	v_fmamk_f32 v64, v112, 0x3d000000, v208
	v_fmamk_f32 v108, v108, 0x3d000000, v200
	v_addc_co_u32_e32 v119, vcc, 0, v67, vcc
	v_min_f32_e32 v64, 0x40e00000, v64
	v_min_f32_e32 v108, 0x40e00000, v108
	global_store_dwordx2 v[118:119], v[116:117], off
	v_mul_f32_e32 v112, 0x3fd9db23, v64
	v_mul_f32_e32 v116, 0x3fd9db23, v108
	v_mul_f32_e32 v112, 0xbfb8aa3b, v112
	v_mul_f32_e32 v116, 0xbfb8aa3b, v116
	v_exp_f32_e32 v112, v112
	v_exp_f32_e32 v116, v116
	v_fmamk_f32 v104, v104, 0x3d000000, v204
	v_med3_f32 v104, v104, s71, v235
	v_add_f32_e32 v104, 1.0, v104
	v_add_f32_e32 v112, 1.0, v112
	v_mul_f32_e32 v64, v64, v104
	v_add_f32_e32 v104, 1.0, v116
	v_rcp_f32_e32 v112, v112
	v_fmamk_f32 v100, v100, 0x3d000000, v196
	v_rcp_f32_e32 v104, v104
	v_med3_f32 v100, v100, s71, v235
	v_add_f32_e32 v100, 1.0, v100
	v_fmamk_f32 v109, v109, 0x3d000000, v201
	v_mul_f32_e32 v100, v108, v100
	v_min_f32_e32 v109, 0x40e00000, v109
	v_mul_f32_e32 v64, v64, v112
	v_mul_f32_e32 v104, v100, v104
	v_fmamk_f32 v100, v113, 0x3d000000, v209
	v_mul_f32_e32 v112, 0x3fd9db23, v109
	v_min_f32_e32 v100, 0x40e00000, v100
	v_mul_f32_e32 v112, 0xbfb8aa3b, v112
	v_mul_f32_e32 v108, 0x3fd9db23, v100
	v_exp_f32_e32 v112, v112
	v_mul_f32_e32 v108, 0xbfb8aa3b, v108
	v_fmamk_f32 v105, v105, 0x3d000000, v205
	v_exp_f32_e32 v108, v108
	v_med3_f32 v105, v105, s71, v235
	v_add_f32_e32 v105, 1.0, v105
	v_mul_f32_e32 v100, v100, v105
	v_fmamk_f32 v101, v101, 0x3d000000, v197
	v_add_f32_e32 v105, 1.0, v112
	v_rcp_f32_e32 v105, v105
	v_med3_f32 v101, v101, s71, v235
	v_add_f32_e32 v108, 1.0, v108
	v_add_f32_e32 v101, 1.0, v101
	v_rcp_f32_e32 v108, v108
	v_mul_f32_e32 v101, v109, v101
	v_fmamk_f32 v109, v110, 0x3d000000, v202
	v_min_f32_e32 v109, 0x40e00000, v109
	v_mul_f32_e32 v101, v101, v105
	v_fmamk_f32 v105, v114, 0x3d000000, v210
	v_mul_f32_e32 v110, 0x3fd9db23, v109
; __device__ __forceinline__ float sigmoidf_(float x) { return __builtin_amdgcn_rcpf(1.f + __expf(-x)); }
;     __device__ __forceinline__ void operator()(const g8::Acc& acc, const g8::Unit& u, int wr, int wc, int fr, int fq) const {
;         const int row0 = u.pm * 256 + wr * 64 + fr, j0 = u.pn * 128 + wc * 32 + 8 * fq;
;         const float* bg = bgu + (size_t)u.e * 4096 + j0; const float* bu = bg + 2048;
;         const f32x4 g0 = *(const f32x4*)bg, g1 = *(const f32x4*)(bg + 4), u0 = *(const f32x4*)bu, u1 = *(const f32x4*)(bu + 4);
; #pragma unroll
;         for (int ai = 0; ai < 2; ++ai) {
;             if (u.hm <= ai * 128 + wr * 64) break;
; #pragma unroll
;             for (int m = 0; m < 4; ++m) {
;                 f32x4 ga = acc[ai][0][m][0] * WINV + g0, gb = acc[ai][0][m][1] * WINV + g1, ua = acc[ai][1][m][0] * WINV + u0, ub = acc[ai][1][m][1] * WINV + u1;
;                 f32x4 ha, hb;
; #pragma unroll
;                 for (int j = 0; j < 4; ++j) {
;                     const float gt = fminf(ga[j], 7.f), up = fminf(fmaxf(ua[j], -7.f), 7.f);
;                     ha[j] = (up + 1.f) * gt * sigmoidf_(1.702f * gt);
;                     const float gt2 = fminf(gb[j], 7.f), up2 = fminf(fmaxf(ub[j], -7.f), 7.f);
;                     hb[j] = (up2 + 1.f) * gt2 * sigmoidf_(1.702f * gt2);
;                 }
;                 u32x2 w; w.x = pk4_fp8s(ha[0], ha[1], ha[2], ha[3]); w.y = pk4_fp8s(hb[0], hb[1], hb[2], hb[3]);
;                 *(u32x2*)(HID + (size_t)(row0 + ai * 128 + m * 16) * 2048 + j0) = w;
;             }
;         }
	v_min_f32_e32 v105, 0x40e00000, v105
	v_mul_f32_e32 v110, 0xbfb8aa3b, v110
	v_mul_f32_e32 v100, v100, v108
	v_mul_f32_e32 v108, 0x3fd9db23, v105
	v_exp_f32_e32 v110, v110
	v_mul_f32_e32 v108, 0xbfb8aa3b, v108
	v_fmamk_f32 v106, v106, 0x3d000000, v206
	v_exp_f32_e32 v108, v108
	v_med3_f32 v106, v106, s71, v235
	v_fmamk_f32 v102, v102, 0x3d000000, v198
	v_add_f32_e32 v106, 1.0, v106
	v_med3_f32 v102, v102, s71, v235
	v_mul_f32_e32 v105, v105, v106
	v_add_f32_e32 v106, 1.0, v110
	v_add_f32_e32 v102, 1.0, v102
	v_rcp_f32_e32 v106, v106
	v_mul_f32_e32 v102, v109, v102
	v_fmamk_f32 v109, v111, 0x3d000000, v203
	v_add_f32_e32 v108, 1.0, v108
	v_min_f32_e32 v109, 0x40e00000, v109
	v_rcp_f32_e32 v108, v108
	v_mul_f32_e32 v110, 0x3fd9db23, v109
	v_mul_f32_e32 v110, 0xbfb8aa3b, v110
	v_mul_f32_e32 v102, v102, v106
	v_fmamk_f32 v106, v115, 0x3d000000, v211
	v_exp_f32_e32 v110, v110
	v_min_f32_e32 v106, 0x40e00000, v106
	v_fmamk_f32 v107, v107, 0x3d000000, v207
	v_mul_f32_e32 v105, v105, v108
	v_mul_f32_e32 v108, 0x3fd9db23, v106
	v_med3_f32 v107, v107, s71, v235
	v_mul_f32_e32 v108, 0xbfb8aa3b, v108
	v_add_f32_e32 v107, 1.0, v107
	v_exp_f32_e32 v108, v108
	v_mul_f32_e32 v106, v106, v107
	v_add_f32_e32 v107, 1.0, v110
	v_fmamk_f32 v103, v103, 0x3d000000, v199
	v_rcp_f32_e32 v107, v107
	v_med3_f32 v103, v103, s71, v235
	v_add_f32_e32 v103, 1.0, v103
	v_add_f32_e32 v108, 1.0, v108
	v_mul_f32_e32 v103, v109, v103
	v_rcp_f32_e32 v108, v108
	v_mul_f32_e32 v103, v103, v107
	v_med3_f32 v64, v64, s72, v236
	v_med3_f32 v107, v100, s72, v236
	v_mov_b32_e32 v100, v65
	v_cvt_pk_fp8_f32 v100, v64, v107
	v_med3_f32 v64, v104, s72, v236
	v_med3_f32 v104, v101, s72, v236
	v_mov_b32_e32 v101, v65
	v_cvt_pk_fp8_f32 v101, v64, v104
	v_mul_f32_e32 v106, v106, v108
	v_med3_f32 v105, v105, s72, v236
	v_med3_f32 v106, v106, s72, v236
	v_med3_f32 v64, v102, s72, v236
	v_med3_f32 v102, v103, s72, v236
	v_cvt_pk_fp8_f32 v100, v105, v106 op_sel:[0,0,1]
	v_cvt_pk_fp8_f32 v101, v64, v102 op_sel:[0,0,1]
	v_add_co_u32_e32 v102, vcc, s48, v66
	v_fmamk_f32 v64, v96, 0x3d000000, v208
	v_fmamk_f32 v92, v92, 0x3d000000, v200
	v_addc_co_u32_e32 v103, vcc, 0, v67, vcc
	v_min_f32_e32 v64, 0x40e00000, v64
	v_min_f32_e32 v92, 0x40e00000, v92
	global_store_dwordx2 v[102:103], v[100:101], off
	v_mul_f32_e32 v96, 0x3fd9db23, v64
	v_mul_f32_e32 v100, 0x3fd9db23, v92
	v_mul_f32_e32 v96, 0xbfb8aa3b, v96
	v_mul_f32_e32 v100, 0xbfb8aa3b, v100
	v_exp_f32_e32 v96, v96
	v_exp_f32_e32 v100, v100
	v_fmamk_f32 v88, v88, 0x3d000000, v204
	v_med3_f32 v88, v88, s71, v235
	v_add_f32_e32 v88, 1.0, v88
	v_add_f32_e32 v96, 1.0, v96
	v_mul_f32_e32 v64, v64, v88
	v_add_f32_e32 v88, 1.0, v100
	v_rcp_f32_e32 v96, v96
	v_fmamk_f32 v84, v84, 0x3d000000, v196
	v_rcp_f32_e32 v88, v88
	v_med3_f32 v84, v84, s71, v235
	v_add_f32_e32 v84, 1.0, v84
	v_fmamk_f32 v93, v93, 0x3d000000, v201
	v_mul_f32_e32 v84, v92, v84
	v_min_f32_e32 v93, 0x40e00000, v93
	v_mul_f32_e32 v64, v64, v96
	v_mul_f32_e32 v88, v84, v88
	v_fmamk_f32 v84, v97, 0x3d000000, v209
	v_mul_f32_e32 v96, 0x3fd9db23, v93
	v_min_f32_e32 v84, 0x40e00000, v84
	v_mul_f32_e32 v96, 0xbfb8aa3b, v96
	v_mul_f32_e32 v92, 0x3fd9db23, v84
	v_exp_f32_e32 v96, v96
	v_mul_f32_e32 v92, 0xbfb8aa3b, v92
	v_fmamk_f32 v89, v89, 0x3d000000, v205
	v_exp_f32_e32 v92, v92
	v_med3_f32 v89, v89, s71, v235
	v_add_f32_e32 v89, 1.0, v89
	v_mul_f32_e32 v84, v84, v89
	v_fmamk_f32 v85, v85, 0x3d000000, v197
	v_add_f32_e32 v89, 1.0, v96
	v_rcp_f32_e32 v89, v89
	v_med3_f32 v85, v85, s71, v235
	v_add_f32_e32 v92, 1.0, v92
	v_add_f32_e32 v85, 1.0, v85
	v_rcp_f32_e32 v92, v92
	v_mul_f32_e32 v85, v93, v85
	v_fmamk_f32 v93, v94, 0x3d000000, v202
	v_min_f32_e32 v93, 0x40e00000, v93
	v_mul_f32_e32 v85, v85, v89
	v_fmamk_f32 v89, v98, 0x3d000000, v210
	v_mul_f32_e32 v94, 0x3fd9db23, v93
	v_min_f32_e32 v89, 0x40e00000, v89
	v_mul_f32_e32 v94, 0xbfb8aa3b, v94
	v_mul_f32_e32 v84, v84, v92
	v_mul_f32_e32 v92, 0x3fd9db23, v89
	v_exp_f32_e32 v94, v94
	v_mul_f32_e32 v92, 0xbfb8aa3b, v92
	v_fmamk_f32 v90, v90, 0x3d000000, v206
	v_exp_f32_e32 v92, v92
	v_med3_f32 v90, v90, s71, v235
	v_fmamk_f32 v86, v86, 0x3d000000, v198
	v_add_f32_e32 v90, 1.0, v90
	v_med3_f32 v86, v86, s71, v235
	v_mul_f32_e32 v89, v89, v90
	v_add_f32_e32 v90, 1.0, v94
	v_add_f32_e32 v86, 1.0, v86
	v_rcp_f32_e32 v90, v90
	v_mul_f32_e32 v86, v93, v86
	v_fmamk_f32 v93, v95, 0x3d000000, v203
	v_add_f32_e32 v92, 1.0, v92
	v_min_f32_e32 v93, 0x40e00000, v93
	v_rcp_f32_e32 v92, v92
	v_mul_f32_e32 v94, 0x3fd9db23, v93
	v_mul_f32_e32 v94, 0xbfb8aa3b, v94
	v_mul_f32_e32 v86, v86, v90
	v_fmamk_f32 v90, v99, 0x3d000000, v211
	v_exp_f32_e32 v94, v94
	v_min_f32_e32 v90, 0x40e00000, v90
	v_fmamk_f32 v91, v91, 0x3d000000, v207
	v_mul_f32_e32 v89, v89, v92
	v_mul_f32_e32 v92, 0x3fd9db23, v90
	v_med3_f32 v91, v91, s71, v235
	v_mul_f32_e32 v92, 0xbfb8aa3b, v92
	v_add_f32_e32 v91, 1.0, v91
	v_exp_f32_e32 v92, v92
	v_mul_f32_e32 v90, v90, v91
	v_add_f32_e32 v91, 1.0, v94
	v_fmamk_f32 v87, v87, 0x3d000000, v199
	v_rcp_f32_e32 v91, v91
	v_med3_f32 v87, v87, s71, v235
	v_add_f32_e32 v87, 1.0, v87
	v_add_f32_e32 v92, 1.0, v92
	v_mul_f32_e32 v87, v93, v87
	v_rcp_f32_e32 v92, v92
	v_mul_f32_e32 v87, v87, v91
	v_med3_f32 v64, v64, s72, v236
	v_med3_f32 v91, v84, s72, v236
	v_mov_b32_e32 v84, v65
	v_cvt_pk_fp8_f32 v84, v64, v91
	v_med3_f32 v64, v88, s72, v236
	v_med3_f32 v88, v85, s72, v236
	v_mov_b32_e32 v85, v65
	v_cvt_pk_fp8_f32 v85, v64, v88
	v_mul_f32_e32 v90, v90, v92
	v_med3_f32 v89, v89, s72, v236
	v_med3_f32 v90, v90, s72, v236
	v_med3_f32 v64, v86, s72, v236
	v_med3_f32 v86, v87, s72, v236
	v_cvt_pk_fp8_f32 v84, v89, v90 op_sel:[0,0,1]
; __device__ __forceinline__ float sigmoidf_(float x) { return __builtin_amdgcn_rcpf(1.f + __expf(-x)); }
;     __device__ __forceinline__ void operator()(const g8::Acc& acc, const g8::Unit& u, int wr, int wc, int fr, int fq) const {
;         const int row0 = u.pm * 256 + wr * 64 + fr, j0 = u.pn * 128 + wc * 32 + 8 * fq;
;         const float* bg = bgu + (size_t)u.e * 4096 + j0; const float* bu = bg + 2048;
;         const f32x4 g0 = *(const f32x4*)bg, g1 = *(const f32x4*)(bg + 4), u0 = *(const f32x4*)bu, u1 = *(const f32x4*)(bu + 4);
; #pragma unroll
;         for (int ai = 0; ai < 2; ++ai) {
;             if (u.hm <= ai * 128 + wr * 64) break;
; #pragma unroll
;             for (int m = 0; m < 4; ++m) {
;                 f32x4 ga = acc[ai][0][m][0] * WINV + g0, gb = acc[ai][0][m][1] * WINV + g1, ua = acc[ai][1][m][0] * WINV + u0, ub = acc[ai][1][m][1] * WINV + u1;
;                 f32x4 ha, hb;
; #pragma unroll
;                 for (int j = 0; j < 4; ++j) {
;                     const float gt = fminf(ga[j], 7.f), up = fminf(fmaxf(ua[j], -7.f), 7.f);
;                     ha[j] = (up + 1.f) * gt * sigmoidf_(1.702f * gt);
;                     const float gt2 = fminf(gb[j], 7.f), up2 = fminf(fmaxf(ub[j], -7.f), 7.f);
;                     hb[j] = (up2 + 1.f) * gt2 * sigmoidf_(1.702f * gt2);
;                 }
;                 u32x2 w; w.x = pk4_fp8s(ha[0], ha[1], ha[2], ha[3]); w.y = pk4_fp8s(hb[0], hb[1], hb[2], hb[3]);
;                 *(u32x2*)(HID + (size_t)(row0 + ai * 128 + m * 16) * 2048 + j0) = w;
;             }
;         }
	v_cvt_pk_fp8_f32 v85, v64, v86 op_sel:[0,0,1]
	v_add_co_u32_e32 v86, vcc, s49, v66
	v_fmamk_f32 v64, v80, 0x3d000000, v208
	v_fmamk_f32 v76, v76, 0x3d000000, v200
	v_addc_co_u32_e32 v87, vcc, 0, v67, vcc
	v_min_f32_e32 v64, 0x40e00000, v64
	v_min_f32_e32 v76, 0x40e00000, v76
	global_store_dwordx2 v[86:87], v[84:85], off
	v_mul_f32_e32 v80, 0x3fd9db23, v64
	v_mul_f32_e32 v84, 0x3fd9db23, v76
	v_mul_f32_e32 v80, 0xbfb8aa3b, v80
	v_mul_f32_e32 v84, 0xbfb8aa3b, v84
	v_exp_f32_e32 v80, v80
	v_exp_f32_e32 v84, v84
	v_fmamk_f32 v72, v72, 0x3d000000, v204
	v_med3_f32 v72, v72, s71, v235
	v_add_f32_e32 v72, 1.0, v72
	v_add_f32_e32 v80, 1.0, v80
	v_mul_f32_e32 v64, v64, v72
	v_add_f32_e32 v72, 1.0, v84
	v_rcp_f32_e32 v80, v80
	v_fmamk_f32 v68, v68, 0x3d000000, v196
	v_rcp_f32_e32 v72, v72
	v_med3_f32 v68, v68, s71, v235
	v_add_f32_e32 v68, 1.0, v68
	v_fmamk_f32 v77, v77, 0x3d000000, v201
	v_mul_f32_e32 v68, v76, v68
	v_min_f32_e32 v77, 0x40e00000, v77
	v_mul_f32_e32 v64, v64, v80
	v_mul_f32_e32 v72, v68, v72
	v_fmamk_f32 v68, v81, 0x3d000000, v209
	v_mul_f32_e32 v80, 0x3fd9db23, v77
	v_min_f32_e32 v68, 0x40e00000, v68
	v_mul_f32_e32 v80, 0xbfb8aa3b, v80
	v_mul_f32_e32 v76, 0x3fd9db23, v68
	v_exp_f32_e32 v80, v80
	v_mul_f32_e32 v76, 0xbfb8aa3b, v76
	v_fmamk_f32 v73, v73, 0x3d000000, v205
	v_exp_f32_e32 v76, v76
	v_med3_f32 v73, v73, s71, v235
	v_add_f32_e32 v73, 1.0, v73
	v_mul_f32_e32 v68, v68, v73
	v_add_f32_e32 v73, 1.0, v80
	v_fmamk_f32 v69, v69, 0x3d000000, v197
	v_rcp_f32_e32 v73, v73
	v_add_f32_e32 v76, 1.0, v76
	v_med3_f32 v69, v69, s71, v235
	v_rcp_f32_e32 v76, v76
	v_add_f32_e32 v69, 1.0, v69
	v_mul_f32_e32 v69, v77, v69
	v_fmamk_f32 v77, v78, 0x3d000000, v202
	v_mul_f32_e32 v69, v69, v73
	v_fmamk_f32 v73, v82, 0x3d000000, v210
	v_min_f32_e32 v77, 0x40e00000, v77
	v_min_f32_e32 v73, 0x40e00000, v73
	v_mul_f32_e32 v78, 0x3fd9db23, v77
	v_mul_f32_e32 v68, v68, v76
	v_mul_f32_e32 v76, 0x3fd9db23, v73
	v_mul_f32_e32 v78, 0xbfb8aa3b, v78
	v_mul_f32_e32 v76, 0xbfb8aa3b, v76
	v_exp_f32_e32 v78, v78
	v_exp_f32_e32 v76, v76
	v_fmamk_f32 v74, v74, 0x3d000000, v206
	v_med3_f32 v74, v74, s71, v235
	v_fmamk_f32 v70, v70, 0x3d000000, v198
	v_add_f32_e32 v74, 1.0, v74
	v_med3_f32 v70, v70, s71, v235
	v_mul_f32_e32 v73, v73, v74
	v_add_f32_e32 v74, 1.0, v78
	v_add_f32_e32 v70, 1.0, v70
	v_fmac_f32_e32 v203, 0x3d000000, v79
	v_add_f32_e32 v76, 1.0, v76
	v_rcp_f32_e32 v74, v74
	v_mul_f32_e32 v70, v77, v70
	v_min_f32_e32 v77, 0x40e00000, v203
	v_rcp_f32_e32 v76, v76
	v_mul_f32_e32 v78, 0x3fd9db23, v77
	v_mul_f32_e32 v78, 0xbfb8aa3b, v78
	v_fmac_f32_e32 v211, 0x3d000000, v83
	v_exp_f32_e32 v78, v78
	v_mul_f32_e32 v70, v70, v74
	v_min_f32_e32 v74, 0x40e00000, v211
	v_mul_f32_e32 v73, v73, v76
	v_mul_f32_e32 v76, 0x3fd9db23, v74
	v_mul_f32_e32 v76, 0xbfb8aa3b, v76
	v_fmac_f32_e32 v207, 0x3d000000, v75
	v_exp_f32_e32 v76, v76
	v_med3_f32 v75, v207, s71, v235
	v_fmac_f32_e32 v199, 0x3d000000, v71
	v_add_f32_e32 v71, 1.0, v78
	v_add_f32_e32 v75, 1.0, v75
	v_rcp_f32_e32 v71, v71
	v_mul_f32_e32 v74, v74, v75
	v_med3_f32 v75, v199, s71, v235
	v_add_f32_e32 v75, 1.0, v75
	v_add_f32_e32 v76, 1.0, v76
	v_mul_f32_e32 v75, v77, v75
	v_rcp_f32_e32 v76, v76
	v_mul_f32_e32 v71, v75, v71
	v_med3_f32 v64, v64, s72, v236
	v_med3_f32 v75, v68, s72, v236
	v_mov_b32_e32 v68, v65
	v_cvt_pk_fp8_f32 v68, v64, v75
	v_med3_f32 v64, v72, s72, v236
	v_med3_f32 v72, v69, s72, v236
	v_mov_b32_e32 v69, v65
	v_cvt_pk_fp8_f32 v69, v64, v72
	v_mul_f32_e32 v74, v74, v76
	v_med3_f32 v73, v73, s72, v236
	v_med3_f32 v74, v74, s72, v236
	v_med3_f32 v64, v70, s72, v236
	v_med3_f32 v70, v71, s72, v236
	v_cvt_pk_fp8_f32 v68, v73, v74 op_sel:[0,0,1]
	v_cvt_pk_fp8_f32 v69, v64, v70 op_sel:[0,0,1]
	v_add_co_u32_e32 v66, vcc, 0x58000, v66
	s_nop 1
	v_addc_co_u32_e32 v67, vcc, 0, v67, vcc
	global_store_dwordx2 v[66:67], v[68:69], off
	s_cmp_eq_u32 s99, 0
	s_cbranch_scc1 .Lp9f8_nofin
	s_sub_i32 s100, s99, 0x10000
	s_lshr_b32 s100, s100, 10
	s_lshl_b32 s100, s100, 22
	s_and_b32 s101, s99, 63
	s_lshl_b32 s101, s101, 16
	s_add_i32 s100, s100, s101
	s_bfe_u32 s101, s99, 0x40006
	s_lshl_b32 s101, s101, 7
	s_add_i32 s100, s100, s101
	v_mbcnt_lo_u32_b32 v244, -1, 0
	v_mbcnt_hi_u32_b32 v244, -1, v244
	v_lshrrev_b32_e32 v245, 3, v244
	v_and_b32_e32 v246, 7, v244
	v_lshlrev_b32_e32 v245, 4, v245
	v_lshl_or_b32 v245, v246, 13, v245
	v_add_u32_e32 v245, s100, v245
	v_readlane_b32 s100, v254, 48
	v_readlane_b32 s101, v254, 49
	s_add_u32 s100, s100, 0x14d59400
	s_addc_u32 s101, s101, 0
	s_waitcnt vmcnt(8)
	v_mul_f32_e32 v246, 0x42000000, v0
	v_mul_f32_e32 v247, 0x42000000, v4
	v_mov_b32_e32 v248, 0
	v_cvt_pk_fp8_f32 v248, v246, v247
	v_mul_f32_e32 v246, 0x42000000, v8
	v_mul_f32_e32 v247, 0x42000000, v12
	v_cvt_pk_fp8_f32 v248, v246, v247 op_sel:[0,0,1]
	v_mul_f32_e32 v246, 0x42000000, v16
	v_mul_f32_e32 v247, 0x42000000, v20
	v_mov_b32_e32 v249, 0
	v_cvt_pk_fp8_f32 v249, v246, v247
	v_mul_f32_e32 v246, 0x42000000, v24
	v_mul_f32_e32 v247, 0x42000000, v28
	v_cvt_pk_fp8_f32 v249, v246, v247 op_sel:[0,0,1]
	v_mul_f32_e32 v246, 0x42000000, v32
	v_mul_f32_e32 v247, 0x42000000, v36
	v_mov_b32_e32 v250, 0
	v_cvt_pk_fp8_f32 v250, v246, v247
	v_mul_f32_e32 v246, 0x42000000, v40
	v_mul_f32_e32 v247, 0x42000000, v44
	v_cvt_pk_fp8_f32 v250, v246, v247 op_sel:[0,0,1]
	v_mul_f32_e32 v246, 0x42000000, v48
	v_mul_f32_e32 v247, 0x42000000, v52
	v_mov_b32_e32 v251, 0
	v_cvt_pk_fp8_f32 v251, v246, v247
	v_mul_f32_e32 v246, 0x42000000, v56
	v_mul_f32_e32 v247, 0x42000000, v60
	v_cvt_pk_fp8_f32 v251, v246, v247 op_sel:[0,0,1]
	s_nop 0
	global_store_dwordx4 v245, v[248:251], s[100:101] nt
	v_mul_f32_e32 v246, 0x42000000, v1
	v_mul_f32_e32 v247, 0x42000000, v5
	v_mov_b32_e32 v248, 0
	v_cvt_pk_fp8_f32 v248, v246, v247
	v_mul_f32_e32 v246, 0x42000000, v9
	v_mul_f32_e32 v247, 0x42000000, v13
	v_cvt_pk_fp8_f32 v248, v246, v247 op_sel:[0,0,1]
	v_mul_f32_e32 v246, 0x42000000, v17
	v_mul_f32_e32 v247, 0x42000000, v21
	v_mov_b32_e32 v249, 0
	v_cvt_pk_fp8_f32 v249, v246, v247
	v_mul_f32_e32 v246, 0x42000000, v25
	v_mul_f32_e32 v247, 0x42000000, v29
	v_cvt_pk_fp8_f32 v249, v246, v247 op_sel:[0,0,1]
	v_mul_f32_e32 v246, 0x42000000, v33
	v_mul_f32_e32 v247, 0x42000000, v37
	v_mov_b32_e32 v250, 0
	v_cvt_pk_fp8_f32 v250, v246, v247
	v_mul_f32_e32 v246, 0x42000000, v41
	v_mul_f32_e32 v247, 0x42000000, v45
	v_cvt_pk_fp8_f32 v250, v246, v247 op_sel:[0,0,1]
	v_mul_f32_e32 v246, 0x42000000, v49
	v_mul_f32_e32 v247, 0x42000000, v53
	v_mov_b32_e32 v251, 0
	v_cvt_pk_fp8_f32 v251, v246, v247
	v_mul_f32_e32 v246, 0x42000000, v57
	v_mul_f32_e32 v247, 0x42000000, v61
	v_cvt_pk_fp8_f32 v251, v246, v247 op_sel:[0,0,1]
	s_nop 0
	global_store_dwordx4 v245, v[248:251], s[100:101] offset:2048 nt
	v_add_u32_e32 v245, 0x1000, v245
	v_mul_f32_e32 v246, 0x42000000, v2
	v_mul_f32_e32 v247, 0x42000000, v6
	v_mov_b32_e32 v248, 0
	v_cvt_pk_fp8_f32 v248, v246, v247
	v_mul_f32_e32 v246, 0x42000000, v10
	v_mul_f32_e32 v247, 0x42000000, v14
	v_cvt_pk_fp8_f32 v248, v246, v247 op_sel:[0,0,1]
	v_mul_f32_e32 v246, 0x42000000, v18
	v_mul_f32_e32 v247, 0x42000000, v22
	v_mov_b32_e32 v249, 0
	v_cvt_pk_fp8_f32 v249, v246, v247
	v_mul_f32_e32 v246, 0x42000000, v26
	v_mul_f32_e32 v247, 0x42000000, v30
	v_cvt_pk_fp8_f32 v249, v246, v247 op_sel:[0,0,1]
	v_mul_f32_e32 v246, 0x42000000, v34
	v_mul_f32_e32 v247, 0x42000000, v38
	v_mov_b32_e32 v250, 0
	v_cvt_pk_fp8_f32 v250, v246, v247
	v_mul_f32_e32 v246, 0x42000000, v42
	v_mul_f32_e32 v247, 0x42000000, v46
	v_cvt_pk_fp8_f32 v250, v246, v247 op_sel:[0,0,1]
	v_mul_f32_e32 v246, 0x42000000, v50
	v_mul_f32_e32 v247, 0x42000000, v54
	v_mov_b32_e32 v251, 0
	v_cvt_pk_fp8_f32 v251, v246, v247
	v_mul_f32_e32 v246, 0x42000000, v58
	v_mul_f32_e32 v247, 0x42000000, v62
	v_cvt_pk_fp8_f32 v251, v246, v247 op_sel:[0,0,1]
	s_nop 0
	global_store_dwordx4 v245, v[248:251], s[100:101] nt
	v_mul_f32_e32 v246, 0x42000000, v3
	v_mul_f32_e32 v247, 0x42000000, v7
	v_mov_b32_e32 v248, 0
	v_cvt_pk_fp8_f32 v248, v246, v247
	v_mul_f32_e32 v246, 0x42000000, v11
	v_mul_f32_e32 v247, 0x42000000, v15
	v_cvt_pk_fp8_f32 v248, v246, v247 op_sel:[0,0,1]
	v_mul_f32_e32 v246, 0x42000000, v19
	v_mul_f32_e32 v247, 0x42000000, v23
	v_mov_b32_e32 v249, 0
	v_cvt_pk_fp8_f32 v249, v246, v247
	v_mul_f32_e32 v246, 0x42000000, v27
	v_mul_f32_e32 v247, 0x42000000, v31
	v_cvt_pk_fp8_f32 v249, v246, v247 op_sel:[0,0,1]
	v_mul_f32_e32 v246, 0x42000000, v35
	v_mul_f32_e32 v247, 0x42000000, v39
	v_mov_b32_e32 v250, 0
	v_cvt_pk_fp8_f32 v250, v246, v247
	v_mul_f32_e32 v246, 0x42000000, v43
	v_mul_f32_e32 v247, 0x42000000, v47
	v_cvt_pk_fp8_f32 v250, v246, v247 op_sel:[0,0,1]
	v_mul_f32_e32 v246, 0x42000000, v51
	v_mul_f32_e32 v247, 0x42000000, v55
	v_mov_b32_e32 v251, 0
	v_cvt_pk_fp8_f32 v251, v246, v247
	v_mul_f32_e32 v246, 0x42000000, v59
	v_mul_f32_e32 v247, 0x42000000, v63
	v_cvt_pk_fp8_f32 v251, v246, v247 op_sel:[0,0,1]
	s_nop 0
	global_store_dwordx4 v245, v[248:251], s[100:101] offset:2048 nt
	s_add_i32 s98, s98, 0x800
	s_mov_b32 s99, 0

.Lp9_fin4:
	s_cmp_eq_u32 s99, 0
	s_cbranch_scc1 .Lp9f4_nofin
	s_sub_i32 s100, s99, 0x10000
	s_lshr_b32 s100, s100, 10
	s_lshl_b32 s100, s100, 22
	s_and_b32 s101, s99, 63
	s_lshl_b32 s101, s101, 16
	s_add_i32 s100, s100, s101
	s_bfe_u32 s101, s99, 0x40006
	s_lshl_b32 s101, s101, 7
	s_add_i32 s100, s100, s101
	v_mbcnt_lo_u32_b32 v244, -1, 0
	v_mbcnt_hi_u32_b32 v244, -1, v244
	v_lshrrev_b32_e32 v245, 3, v244
	v_and_b32_e32 v246, 7, v244
	v_lshlrev_b32_e32 v245, 4, v245
	v_lshl_or_b32 v245, v246, 13, v245
	v_add_u32_e32 v245, s100, v245
	v_readlane_b32 s100, v254, 48
	v_readlane_b32 s101, v254, 49
	s_add_u32 s100, s100, 0x14d59400
	s_addc_u32 s101, s101, 0
	s_waitcnt vmcnt(4)
	v_mul_f32_e32 v246, 0x42000000, v0
	v_mul_f32_e32 v247, 0x42000000, v4
	v_mov_b32_e32 v248, 0
	v_cvt_pk_fp8_f32 v248, v246, v247
	v_mul_f32_e32 v246, 0x42000000, v8
	v_mul_f32_e32 v247, 0x42000000, v12
	v_cvt_pk_fp8_f32 v248, v246, v247 op_sel:[0,0,1]
	v_mul_f32_e32 v246, 0x42000000, v16
	v_mul_f32_e32 v247, 0x42000000, v20
	v_mov_b32_e32 v249, 0
	v_cvt_pk_fp8_f32 v249, v246, v247
	v_mul_f32_e32 v246, 0x42000000, v24
	v_mul_f32_e32 v247, 0x42000000, v28
	v_cvt_pk_fp8_f32 v249, v246, v247 op_sel:[0,0,1]
	v_mul_f32_e32 v246, 0x42000000, v32
	v_mul_f32_e32 v247, 0x42000000, v36
	v_mov_b32_e32 v250, 0
	v_cvt_pk_fp8_f32 v250, v246, v247
	v_mul_f32_e32 v246, 0x42000000, v40
	v_mul_f32_e32 v247, 0x42000000, v44
	v_cvt_pk_fp8_f32 v250, v246, v247 op_sel:[0,0,1]
	v_mul_f32_e32 v246, 0x42000000, v48
	v_mul_f32_e32 v247, 0x42000000, v52
	v_mov_b32_e32 v251, 0
	v_cvt_pk_fp8_f32 v251, v246, v247
	v_mul_f32_e32 v246, 0x42000000, v56
	v_mul_f32_e32 v247, 0x42000000, v60
	v_cvt_pk_fp8_f32 v251, v246, v247 op_sel:[0,0,1]
	s_nop 0
	global_store_dwordx4 v245, v[248:251], s[100:101] nt
	v_mul_f32_e32 v246, 0x42000000, v1
	v_mul_f32_e32 v247, 0x42000000, v5
	v_mov_b32_e32 v248, 0
	v_cvt_pk_fp8_f32 v248, v246, v247
	v_mul_f32_e32 v246, 0x42000000, v9
	v_mul_f32_e32 v247, 0x42000000, v13
	v_cvt_pk_fp8_f32 v248, v246, v247 op_sel:[0,0,1]
	v_mul_f32_e32 v246, 0x42000000, v17
	v_mul_f32_e32 v247, 0x42000000, v21
	v_mov_b32_e32 v249, 0
	v_cvt_pk_fp8_f32 v249, v246, v247
	v_mul_f32_e32 v246, 0x42000000, v25
	v_mul_f32_e32 v247, 0x42000000, v29
	v_cvt_pk_fp8_f32 v249, v246, v247 op_sel:[0,0,1]
	v_mul_f32_e32 v246, 0x42000000, v33
	v_mul_f32_e32 v247, 0x42000000, v37
	v_mov_b32_e32 v250, 0
	v_cvt_pk_fp8_f32 v250, v246, v247
	v_mul_f32_e32 v246, 0x42000000, v41
	v_mul_f32_e32 v247, 0x42000000, v45
	v_cvt_pk_fp8_f32 v250, v246, v247 op_sel:[0,0,1]
	v_mul_f32_e32 v246, 0x42000000, v49
	v_mul_f32_e32 v247, 0x42000000, v53
	v_mov_b32_e32 v251, 0
	v_cvt_pk_fp8_f32 v251, v246, v247
	v_mul_f32_e32 v246, 0x42000000, v57
	v_mul_f32_e32 v247, 0x42000000, v61
	v_cvt_pk_fp8_f32 v251, v246, v247 op_sel:[0,0,1]
	s_nop 0
	global_store_dwordx4 v245, v[248:251], s[100:101] offset:2048 nt
	v_add_u32_e32 v245, 0x1000, v245
	v_mul_f32_e32 v246, 0x42000000, v2
	v_mul_f32_e32 v247, 0x42000000, v6
	v_mov_b32_e32 v248, 0
	v_cvt_pk_fp8_f32 v248, v246, v247
	v_mul_f32_e32 v246, 0x42000000, v10
	v_mul_f32_e32 v247, 0x42000000, v14
	v_cvt_pk_fp8_f32 v248, v246, v247 op_sel:[0,0,1]
	v_mul_f32_e32 v246, 0x42000000, v18
	v_mul_f32_e32 v247, 0x42000000, v22
	v_mov_b32_e32 v249, 0
	v_cvt_pk_fp8_f32 v249, v246, v247
	v_mul_f32_e32 v246, 0x42000000, v26
	v_mul_f32_e32 v247, 0x42000000, v30
	v_cvt_pk_fp8_f32 v249, v246, v247 op_sel:[0,0,1]
	v_mul_f32_e32 v246, 0x42000000, v34
	v_mul_f32_e32 v247, 0x42000000, v38
	v_mov_b32_e32 v250, 0
	v_cvt_pk_fp8_f32 v250, v246, v247
	v_mul_f32_e32 v246, 0x42000000, v42
	v_mul_f32_e32 v247, 0x42000000, v46
	v_cvt_pk_fp8_f32 v250, v246, v247 op_sel:[0,0,1]
	v_mul_f32_e32 v246, 0x42000000, v50
	v_mul_f32_e32 v247, 0x42000000, v54
	v_mov_b32_e32 v251, 0
	v_cvt_pk_fp8_f32 v251, v246, v247
	v_mul_f32_e32 v246, 0x42000000, v58
	v_mul_f32_e32 v247, 0x42000000, v62
	v_cvt_pk_fp8_f32 v251, v246, v247 op_sel:[0,0,1]
	s_nop 0
	global_store_dwordx4 v245, v[248:251], s[100:101] nt
	v_mul_f32_e32 v246, 0x42000000, v3
	v_mul_f32_e32 v247, 0x42000000, v7
	v_mov_b32_e32 v248, 0
	v_cvt_pk_fp8_f32 v248, v246, v247
	v_mul_f32_e32 v246, 0x42000000, v11
	v_mul_f32_e32 v247, 0x42000000, v15
	v_cvt_pk_fp8_f32 v248, v246, v247 op_sel:[0,0,1]
	v_mul_f32_e32 v246, 0x42000000, v19
	v_mul_f32_e32 v247, 0x42000000, v23
	v_mov_b32_e32 v249, 0
	v_cvt_pk_fp8_f32 v249, v246, v247
	v_mul_f32_e32 v246, 0x42000000, v27
	v_mul_f32_e32 v247, 0x42000000, v31
	v_cvt_pk_fp8_f32 v249, v246, v247 op_sel:[0,0,1]
	v_mul_f32_e32 v246, 0x42000000, v35
	v_mul_f32_e32 v247, 0x42000000, v39
	v_mov_b32_e32 v250, 0
	v_cvt_pk_fp8_f32 v250, v246, v247
	v_mul_f32_e32 v246, 0x42000000, v43
	v_mul_f32_e32 v247, 0x42000000, v47
	v_cvt_pk_fp8_f32 v250, v246, v247 op_sel:[0,0,1]
	v_mul_f32_e32 v246, 0x42000000, v51
	v_mul_f32_e32 v247, 0x42000000, v55
	v_mov_b32_e32 v251, 0
	v_cvt_pk_fp8_f32 v251, v246, v247
	v_mul_f32_e32 v246, 0x42000000, v59
	v_mul_f32_e32 v247, 0x42000000, v63
	v_cvt_pk_fp8_f32 v251, v246, v247 op_sel:[0,0,1]
	s_nop 0
	global_store_dwordx4 v245, v[248:251], s[100:101] offset:2048 nt
	s_add_i32 s98, s98, 0x800
	s_mov_b32 s99, 0

; __global__ void __launch_bounds__(NTHREADS, 2) fwd(Args args) {
;     ...
;                 f32x4 cv[16];
; #pragma unroll 1
;                 while (cvs.t < ml::T_CONV) { CV_ISSUE(); CV_FINISH(); }
.LBB0_1184:
.Lp9_cl_loop:
	s_cmp_lt_u32 s98, 0x18000
	s_cbranch_scc0 .Lp9_cl_done
	s_mov_b32 s99, s98
	v_mbcnt_lo_u32_b32 v244, -1, 0
	v_mbcnt_hi_u32_b32 v244, -1, v244
	s_sub_i32 s100, s99, 0x10000
	s_lshr_b32 s100, s100, 10
	s_lshl_b32 s100, s100, 24
	s_bfe_u32 s101, s99, 0x40006
	s_lshl_b32 s101, s101, 20
	s_add_i32 s100, s100, s101
	s_and_b32 s101, s99, 63
	s_lshl_b32 s101, s101, 7
	s_add_i32 s100, s100, s101
	v_lshrrev_b32_e32 v245, 3, v244
	v_and_b32_e32 v246, 7, v244
	v_lshlrev_b32_e32 v245, 17, v245
	v_lshl_or_b32 v245, v246, 4, v245
	v_add_u32_e32 v245, s100, v245
	v_readlane_b32 s100, v254, 42
	v_readlane_b32 s101, v254, 43
	s_nop 4
	global_load_dwordx4 v[0:3], v245, s[100:101] nt
	v_add_u32_e32 v245, 0x2000, v245
	global_load_dwordx4 v[4:7], v245, s[100:101] nt
	v_add_u32_e32 v245, 0x2000, v245
	global_load_dwordx4 v[8:11], v245, s[100:101] nt
	v_add_u32_e32 v245, 0x2000, v245
	global_load_dwordx4 v[12:15], v245, s[100:101] nt
	v_add_u32_e32 v245, 0x2000, v245
	global_load_dwordx4 v[16:19], v245, s[100:101] nt
	v_add_u32_e32 v245, 0x2000, v245
	global_load_dwordx4 v[20:23], v245, s[100:101] nt
	v_add_u32_e32 v245, 0x2000, v245
	global_load_dwordx4 v[24:27], v245, s[100:101] nt
	v_add_u32_e32 v245, 0x2000, v245
	global_load_dwordx4 v[28:31], v245, s[100:101] nt
	v_add_u32_e32 v245, 0x2000, v245
	global_load_dwordx4 v[32:35], v245, s[100:101] nt
	v_add_u32_e32 v245, 0x2000, v245
	global_load_dwordx4 v[36:39], v245, s[100:101] nt
	v_add_u32_e32 v245, 0x2000, v245
	global_load_dwordx4 v[40:43], v245, s[100:101] nt
	v_add_u32_e32 v245, 0x2000, v245
	global_load_dwordx4 v[44:47], v245, s[100:101] nt
	v_add_u32_e32 v245, 0x2000, v245
	global_load_dwordx4 v[48:51], v245, s[100:101] nt
	v_add_u32_e32 v245, 0x2000, v245
	global_load_dwordx4 v[52:55], v245, s[100:101] nt
	v_add_u32_e32 v245, 0x2000, v245
	global_load_dwordx4 v[56:59], v245, s[100:101] nt
	v_add_u32_e32 v245, 0x2000, v245
	global_load_dwordx4 v[60:63], v245, s[100:101] nt
	s_sub_i32 s100, s99, 0x10000
	s_lshr_b32 s100, s100, 10
	s_lshl_b32 s100, s100, 22
	s_and_b32 s101, s99, 63
	s_lshl_b32 s101, s101, 16
	s_add_i32 s100, s100, s101
	s_bfe_u32 s101, s99, 0x40006
	s_lshl_b32 s101, s101, 7
	s_add_i32 s100, s100, s101
	v_mbcnt_lo_u32_b32 v244, -1, 0
	v_mbcnt_hi_u32_b32 v244, -1, v244
	v_lshrrev_b32_e32 v245, 3, v244
	v_and_b32_e32 v246, 7, v244
	v_lshlrev_b32_e32 v245, 4, v245
	v_lshl_or_b32 v245, v246, 13, v245
	v_add_u32_e32 v245, s100, v245
	v_readlane_b32 s100, v254, 48
	v_readlane_b32 s101, v254, 49
	s_add_u32 s100, s100, 0x14d59400
	s_addc_u32 s101, s101, 0
	s_waitcnt vmcnt(0)
	v_mul_f32_e32 v246, 0x42000000, v0
	v_mul_f32_e32 v247, 0x42000000, v4
	v_mov_b32_e32 v248, 0
	v_cvt_pk_fp8_f32 v248, v246, v247
	v_mul_f32_e32 v246, 0x42000000, v8
	v_mul_f32_e32 v247, 0x42000000, v12
	v_cvt_pk_fp8_f32 v248, v246, v247 op_sel:[0,0,1]
	v_mul_f32_e32 v246, 0x42000000, v16
	v_mul_f32_e32 v247, 0x42000000, v20
	v_mov_b32_e32 v249, 0
	v_cvt_pk_fp8_f32 v249, v246, v247
	v_mul_f32_e32 v246, 0x42000000, v24
	v_mul_f32_e32 v247, 0x42000000, v28
	v_cvt_pk_fp8_f32 v249, v246, v247 op_sel:[0,0,1]
	v_mul_f32_e32 v246, 0x42000000, v32
	v_mul_f32_e32 v247, 0x42000000, v36
	v_mov_b32_e32 v250, 0
	v_cvt_pk_fp8_f32 v250, v246, v247
	v_mul_f32_e32 v246, 0x42000000, v40
	v_mul_f32_e32 v247, 0x42000000, v44
	v_cvt_pk_fp8_f32 v250, v246, v247 op_sel:[0,0,1]
	v_mul_f32_e32 v246, 0x42000000, v48
	v_mul_f32_e32 v247, 0x42000000, v52
	v_mov_b32_e32 v251, 0
	v_cvt_pk_fp8_f32 v251, v246, v247
	v_mul_f32_e32 v246, 0x42000000, v56
	v_mul_f32_e32 v247, 0x42000000, v60
	v_cvt_pk_fp8_f32 v251, v246, v247 op_sel:[0,0,1]
	s_nop 0
	global_store_dwordx4 v245, v[248:251], s[100:101] nt
	v_mul_f32_e32 v246, 0x42000000, v1
	v_mul_f32_e32 v247, 0x42000000, v5
	v_mov_b32_e32 v248, 0
	v_cvt_pk_fp8_f32 v248, v246, v247
	v_mul_f32_e32 v246, 0x42000000, v9
	v_mul_f32_e32 v247, 0x42000000, v13
	v_cvt_pk_fp8_f32 v248, v246, v247 op_sel:[0,0,1]
	v_mul_f32_e32 v246, 0x42000000, v17
	v_mul_f32_e32 v247, 0x42000000, v21
	v_mov_b32_e32 v249, 0
	v_cvt_pk_fp8_f32 v249, v246, v247
	v_mul_f32_e32 v246, 0x42000000, v25
	v_mul_f32_e32 v247, 0x42000000, v29
	v_cvt_pk_fp8_f32 v249, v246, v247 op_sel:[0,0,1]
	v_mul_f32_e32 v246, 0x42000000, v33
	v_mul_f32_e32 v247, 0x42000000, v37
	v_mov_b32_e32 v250, 0
	v_cvt_pk_fp8_f32 v250, v246, v247
	v_mul_f32_e32 v246, 0x42000000, v41
	v_mul_f32_e32 v247, 0x42000000, v45
	v_cvt_pk_fp8_f32 v250, v246, v247 op_sel:[0,0,1]
	v_mul_f32_e32 v246, 0x42000000, v49
	v_mul_f32_e32 v247, 0x42000000, v53
	v_mov_b32_e32 v251, 0
	v_cvt_pk_fp8_f32 v251, v246, v247
	v_mul_f32_e32 v246, 0x42000000, v57
	v_mul_f32_e32 v247, 0x42000000, v61
	v_cvt_pk_fp8_f32 v251, v246, v247 op_sel:[0,0,1]
	s_nop 0
	global_store_dwordx4 v245, v[248:251], s[100:101] offset:2048 nt
	v_add_u32_e32 v245, 0x1000, v245
	v_mul_f32_e32 v246, 0x42000000, v2
	v_mul_f32_e32 v247, 0x42000000, v6
	v_mov_b32_e32 v248, 0
	v_cvt_pk_fp8_f32 v248, v246, v247
	v_mul_f32_e32 v246, 0x42000000, v10
	v_mul_f32_e32 v247, 0x42000000, v14
	v_cvt_pk_fp8_f32 v248, v246, v247 op_sel:[0,0,1]
	v_mul_f32_e32 v246, 0x42000000, v18
	v_mul_f32_e32 v247, 0x42000000, v22
	v_mov_b32_e32 v249, 0
	v_cvt_pk_fp8_f32 v249, v246, v247
	v_mul_f32_e32 v246, 0x42000000, v26
	v_mul_f32_e32 v247, 0x42000000, v30
	v_cvt_pk_fp8_f32 v249, v246, v247 op_sel:[0,0,1]
	v_mul_f32_e32 v246, 0x42000000, v34
	v_mul_f32_e32 v247, 0x42000000, v38
	v_mov_b32_e32 v250, 0
	v_cvt_pk_fp8_f32 v250, v246, v247
	v_mul_f32_e32 v246, 0x42000000, v42
	v_mul_f32_e32 v247, 0x42000000, v46
	v_cvt_pk_fp8_f32 v250, v246, v247 op_sel:[0,0,1]
	v_mul_f32_e32 v246, 0x42000000, v50
	v_mul_f32_e32 v247, 0x42000000, v54
	v_mov_b32_e32 v251, 0
	v_cvt_pk_fp8_f32 v251, v246, v247
	v_mul_f32_e32 v246, 0x42000000, v58
	v_mul_f32_e32 v247, 0x42000000, v62
	v_cvt_pk_fp8_f32 v251, v246, v247 op_sel:[0,0,1]
	s_nop 0
	global_store_dwordx4 v245, v[248:251], s[100:101] nt
	v_mul_f32_e32 v246, 0x42000000, v3
	v_mul_f32_e32 v247, 0x42000000, v7
	v_mov_b32_e32 v248, 0
	v_cvt_pk_fp8_f32 v248, v246, v247
	v_mul_f32_e32 v246, 0x42000000, v11
	v_mul_f32_e32 v247, 0x42000000, v15
	v_cvt_pk_fp8_f32 v248, v246, v247 op_sel:[0,0,1]
	v_mul_f32_e32 v246, 0x42000000, v19
	v_mul_f32_e32 v247, 0x42000000, v23
	v_mov_b32_e32 v249, 0
	v_cvt_pk_fp8_f32 v249, v246, v247
	v_mul_f32_e32 v246, 0x42000000, v27
	v_mul_f32_e32 v247, 0x42000000, v31
	v_cvt_pk_fp8_f32 v249, v246, v247 op_sel:[0,0,1]
	v_mul_f32_e32 v246, 0x42000000, v35
	v_mul_f32_e32 v247, 0x42000000, v39
	v_mov_b32_e32 v250, 0
	v_cvt_pk_fp8_f32 v250, v246, v247
	v_mul_f32_e32 v246, 0x42000000, v43
	v_mul_f32_e32 v247, 0x42000000, v47
	v_cvt_pk_fp8_f32 v250, v246, v247 op_sel:[0,0,1]
	v_mul_f32_e32 v246, 0x42000000, v51
	v_mul_f32_e32 v247, 0x42000000, v55
	v_mov_b32_e32 v251, 0
	v_cvt_pk_fp8_f32 v251, v246, v247
	v_mul_f32_e32 v246, 0x42000000, v59
	v_mul_f32_e32 v247, 0x42000000, v63
	v_cvt_pk_fp8_f32 v251, v246, v247 op_sel:[0,0,1]
	s_nop 0
	global_store_dwordx4 v245, v[248:251], s[100:101] offset:2048 nt
	s_add_i32 s98, s98, 0x800
	s_mov_b32 s99, 0
	s_branch .Lp9_cl_loop
